# attention key loop: back edge rotated (loop-carried moves and exit test ahead of the loop-back barrier, barrier is the loop head)
# speedup vs baseline: 1.0024x; 1.0024x over previous
; #define SBAR() __builtin_amdgcn_sched_barrier(0)
; __device__ __forceinline__ void attn_unit(const bf16_t* Qb, const unsigned char* Kh, const unsigned char* Vh, bf16_t* Ob, int seq, int cbase, int lbase, int t0, const f32x2* atab, char* lds, const int wave_s) {
;     ...
;     for (int j = 1; j + 1 < NT; j += 2) {
;         { const int bn = 3 - bprev - bj; DMA_TILE(j + 1, bn);
;           SBAR(); qkt(pB0, pB1, m_reg, KBUF(bj), qr, r32, hi);
.LBB0_549:
	s_barrier
	s_mul_i32 s0, s11, 0x5c00
	s_add_i32 s12, s0, 0
	v_add3_u32 v164, s12, v177, v161
	ds_read_b128 v[96:99], v164
	ds_read_b128 v[100:103], v164 offset:16
	ds_read_b128 v[136:139], v164 offset:6656
	ds_read_b128 v[140:143], v164 offset:6672
	s_add_i32 s0, s9, s11
	s_mov_b32 s10, s9
	s_sub_i32 s9, 3, s0
	s_sub_i32 s0, s8, 64
	s_cmp_lt_u32 s13, 3
	s_cselect_b32 s0, s7, s0
	s_mul_hi_i32 s1, s0, 0x300
	s_mulk_i32 s0, 0x300
	s_add_u32 s0, s55, s0
	s_mul_i32 s5, s9, 0x5c00
	s_addc_u32 s1, s56, s1
	s_add_i32 s2, s77, s5
	v_lshl_add_u64 v[166:167], s[0:1], 0, v[152:153]
	s_mov_b32 m0, s2
	s_and_b64 vcc, exec, s[46:47]
	global_load_lds_dwordx4 v[166:167], off
	s_cbranch_vccnz .LBB0_551
	v_lshl_add_u64 v[166:167], s[0:1], 0, v[156:157]
	s_add_i32 m0, s2, 0x2000
	s_nop 0
	global_load_lds_dwordx4 v[166:167], off

; #define SBAR() __builtin_amdgcn_sched_barrier(0)
; #define WAITBAR() do { asm volatile("s_waitcnt vmcnt(0)" ::: "memory"); __syncthreads(); } while (0)
; #define RESC(a) do { if (__any((a) < 1.f)) { if (hi == 0) al_l[r32] = (a); asm volatile("s_waitcnt lgkmcnt(0)" ::: "memory"); \
;     _Pragma("unroll") for (int d = 0; d < 4; ++d) _Pragma("unroll") for (int r = 0; r < 16; ++r) o[d][r] *= al_l[crow(r, hi)]; } } while (0)
; __device__ __forceinline__ void finishSM(f32x16& p0, f32x16& p1, float alpha, float& l_reg, v8i& pa) {
;     ...
;     l_reg = l_reg * alpha + ps;
; __device__ __forceinline__ void attn_unit(const bf16_t* Qb, const unsigned char* Kh, const unsigned char* Vh, bf16_t* Ob, int seq, int cbase, int lbase, int t0, const f32x2* atab, char* lds, const int wave_s) {
;     ...
;           RESC(alB); WAITBAR(); bprev = bj; bj = bn; }
;         { const int bn = 3 - bprev - bj; if (j + 2 < NT) DMA_TILE(j + 2, bn);
;           SBAR(); qkt(pA0, pA1, m_reg, KBUF(bj), qr, r32, hi);
;           finishSM(pB0, pB1, alB, l_reg, pa); SBAR();
;           pv_d0(o, VBASE(bprev), pa, r32, hi); partialSM(pA0, pA1, m_reg, alA, false);
;           RESC(alA); WAITBAR(); bprev = bj; bj = bn; }
;     }
.LBB0_568:
	v_add_f32_e32 v80, v182, v183
	s_waitcnt vmcnt(0)
	s_addk_i32 s7, 0x80
	s_add_i32 s0, s14, 1
	s_addk_i32 s8, 0x80
	v_fmac_f32_e32 v80, v181, v175
	v_add_f32_e32 v175, v217, v218
	s_cmp_ge_i32 s0, s6
	s_mov_b64 s[0:1], 0x5000
	v_fmac_f32_e32 v175, v80, v185
	v_lshl_add_u64 v[158:159], v[158:159], 0, s[0:1]
	s_waitcnt vmcnt(0)
	s_cbranch_scc1 .Lat_exit
	s_mov_b32 s11, s10
	s_mov_b32 s13, s14
	v_mov_b32_e32 v181, v184
	s_branch .LBB0_549
.Lat_exit:
	s_barrier
	s_branch .LBB0_572
